# v7 + hand-written 8-tiles-in-flight prologue weight converter for the 1978 gate/up/down strips
# baseline (speedup 1.0000x reference)
.LBB0_50:
	s_or_b64 exec, exec, s[10:11]
	v_readlane_b32 s0, v251, 2
	s_nop 3
	s_cmpk_lg_u32 s0, 0x100
	s_cbranch_scc1 .Lpc_skip
	v_readlane_b32 s4, v251, 59
	v_readlane_b32 s5, v251, 60
	v_readlane_b32 s48, v251, 31
	v_readlane_b32 s49, v251, 32
	v_readlane_b32 s50, v251, 33
	v_readlane_b32 s51, v251, 34
	v_readlane_b32 s54, v251, 35
	v_readlane_b32 s55, v251, 36
	v_readlane_b32 s27, v251, 3
	v_and_b32_e32 v1, 15, v0
	v_lshrrev_b32_e32 v2, 4, v0
	v_lshlrev_b32_e32 v132, 15, v2
	v_lshl_add_u32 v132, v1, 4, v132
	v_add_u32_e32 v133, 0x2000, v132
	v_add_u32_e32 v134, 0x4000, v132
	v_add_u32_e32 v135, 0x6000, v132
	s_movk_i32 s0, 0x420
	v_mul_u32_u24_e32 v137, s0, v1
	v_lshl_add_u32 v137, v2, 3, v137
	v_lshrrev_b32_e32 v1, 3, v0
	v_and_b32_e32 v2, 7, v0
	s_movk_i32 s0, 0x108
	v_mul_u32_u24_e32 v138, s0, v1
	v_lshl_add_u32 v138, v2, 5, v138
	v_add_u32_e32 v139, 0x4200, v138
	v_lshlrev_b32_e32 v136, 12, v1
	v_lshl_add_u32 v136, v2, 5, v136
	s_sub_i32 s27, 0xff, s27
	s_sub_i32 s0, 0x7b9, s27
	s_lshr_b32 s0, s0, 8
	s_add_i32 s0, s0, 1
	s_lshl_b32 s61, s0, 1
	s_barrier
	s_min_i32 s0, s27, 0x7b9
	s_movk_i32 s1, 0x44c
	s_cmpk_lt_u32 s0, 0x2eb
	s_cselect_b32 s1, 0x2c9, s1
	s_add_i32 s0, s0, s1
	s_cmpk_ge_u32 s0, 0x684
	s_cselect_b32 s9, 1, 0
	s_cselect_b32 s1, 0x684, 0
	s_sub_i32 s0, s0, s1
	s_cmpk_lt_u32 s0, 0x484
	s_cbranch_scc0 .Lpc_d38_wd
	s_sub_u32 s0, s0, 0x84
	s_lshr_b32 s1, s0, 6
	s_and_b32 s0, s0, 63
	s_lshl_b32 s0, s0, 6
	s_lshl_b32 s8, s9, 4
	s_add_i32 s1, s1, s8
	s_lshl_b32 s8, s1, 24
	s_bitcmp1_b32 s0, 7
	s_cselect_b32 s30, s50, s48
	s_cselect_b32 s31, s51, s49
	s_add_u32 s30, s30, s8
	s_addc_u32 s31, s31, 0
	s_lshr_b32 s9, s0, 8
	s_lshl_b32 s9, s9, 7
	s_and_b32 s1, s0, 127
	s_add_i32 s9, s9, s1
	s_lshl_b32 s9, s9, 2
	s_add_u32 s30, s30, s9
	s_addc_u32 s31, s31, 0
	s_add_u32 s34, s4, 0x3c90000
	s_addc_u32 s35, s5, 0
	s_add_u32 s34, s34, s8
	s_addc_u32 s35, s35, 0
	s_lshl_b32 s9, s0, 12
	s_add_u32 s34, s34, s9
	s_addc_u32 s35, s35, 0
	s_branch .Lpc_d38_done
.Lpc_d38_wd:
	s_sub_u32 s0, s0, 0x484
	s_lshr_b32 s1, s0, 5
	s_and_b32 s0, s0, 31
	s_lshl_b32 s0, s0, 6
	s_lshl_b32 s8, s9, 4
	s_add_i32 s1, s1, s8
	s_lshl_b32 s8, s1, 24
	s_add_u32 s30, s54, s8
	s_addc_u32 s31, s55, 0
	s_lshl_b32 s9, s0, 2
	s_add_u32 s30, s30, s9
	s_addc_u32 s31, s31, 0
	s_add_u32 s34, s4, 0x23c90000
	s_addc_u32 s35, s5, 0
	s_lshl_b32 s8, s1, 23
	s_add_u32 s34, s34, s8
	s_addc_u32 s35, s35, 0
	s_lshl_b32 s9, s0, 12
	s_add_u32 s34, s34, s9
	s_addc_u32 s35, s35, 0
.Lpc_d38_done:
	s_mov_b32 s58, 0
	s_add_u32 s62, s30, 0x0
	s_addc_u32 s63, s31, 0
	global_load_dwordx4 v[4:7], v132, s[62:63] nt
	global_load_dwordx4 v[8:11], v133, s[62:63] nt
	global_load_dwordx4 v[12:15], v134, s[62:63] nt
	global_load_dwordx4 v[16:19], v135, s[62:63] nt
	s_add_u32 s62, s30, 0x100000
	s_addc_u32 s63, s31, 0
	global_load_dwordx4 v[20:23], v132, s[62:63] nt
	global_load_dwordx4 v[24:27], v133, s[62:63] nt
	global_load_dwordx4 v[28:31], v134, s[62:63] nt
	global_load_dwordx4 v[32:35], v135, s[62:63] nt
	s_add_u32 s62, s30, 0x200000
	s_addc_u32 s63, s31, 0
	global_load_dwordx4 v[36:39], v132, s[62:63] nt
	global_load_dwordx4 v[40:43], v133, s[62:63] nt
	global_load_dwordx4 v[44:47], v134, s[62:63] nt
	global_load_dwordx4 v[48:51], v135, s[62:63] nt
	s_add_u32 s62, s30, 0x300000
	s_addc_u32 s63, s31, 0
	global_load_dwordx4 v[52:55], v132, s[62:63] nt
	global_load_dwordx4 v[56:59], v133, s[62:63] nt
	global_load_dwordx4 v[60:63], v134, s[62:63] nt
	global_load_dwordx4 v[64:67], v135, s[62:63] nt
	s_add_u32 s62, s30, 0x400000
	s_addc_u32 s63, s31, 0
	global_load_dwordx4 v[68:71], v132, s[62:63] nt
	global_load_dwordx4 v[72:75], v133, s[62:63] nt
	global_load_dwordx4 v[76:79], v134, s[62:63] nt
	global_load_dwordx4 v[80:83], v135, s[62:63] nt
	s_add_u32 s62, s30, 0x500000
	s_addc_u32 s63, s31, 0
	global_load_dwordx4 v[84:87], v132, s[62:63] nt
	global_load_dwordx4 v[88:91], v133, s[62:63] nt
	global_load_dwordx4 v[92:95], v134, s[62:63] nt
	global_load_dwordx4 v[96:99], v135, s[62:63] nt
	s_add_u32 s62, s30, 0x600000
	s_addc_u32 s63, s31, 0
	global_load_dwordx4 v[100:103], v132, s[62:63] nt
	global_load_dwordx4 v[104:107], v133, s[62:63] nt
	global_load_dwordx4 v[108:111], v134, s[62:63] nt
	global_load_dwordx4 v[112:115], v135, s[62:63] nt
	s_add_u32 s62, s30, 0x700000
	s_addc_u32 s63, s31, 0
	global_load_dwordx4 v[116:119], v132, s[62:63] nt
	global_load_dwordx4 v[120:123], v133, s[62:63] nt
	global_load_dwordx4 v[124:127], v134, s[62:63] nt
	global_load_dwordx4 v[128:131], v135, s[62:63] nt
	s_mov_b64 s[32:33], s[34:35]
	s_xor_b32 s58, s58, 1
	s_cmp_eq_u32 s58, 1
	s_cbranch_scc0 .Lpc_a148_new
	s_add_u32 s30, s30, 0x800000
	s_addc_u32 s31, s31, 0
	s_add_u32 s34, s34, 0x800
	s_addc_u32 s35, s35, 0
	s_branch .Lpc_a148_ok
.Lpc_a148_new:
	s_add_i32 s27, s27, 0x100
	s_min_i32 s0, s27, 0x7b9
	s_movk_i32 s1, 0x44c
	s_cmpk_lt_u32 s0, 0x2eb
	s_cselect_b32 s1, 0x2c9, s1
	s_add_i32 s0, s0, s1
	s_cmpk_ge_u32 s0, 0x684
	s_cselect_b32 s9, 1, 0
	s_cselect_b32 s1, 0x684, 0
	s_sub_i32 s0, s0, s1
	s_cmpk_lt_u32 s0, 0x484
	s_cbranch_scc0 .Lpc_d158_wd
	s_sub_u32 s0, s0, 0x84
	s_lshr_b32 s1, s0, 6
	s_and_b32 s0, s0, 63
	s_lshl_b32 s0, s0, 6
	s_lshl_b32 s8, s9, 4
	s_add_i32 s1, s1, s8
	s_lshl_b32 s8, s1, 24
	s_bitcmp1_b32 s0, 7
	s_cselect_b32 s30, s50, s48
	s_cselect_b32 s31, s51, s49
	s_add_u32 s30, s30, s8
	s_addc_u32 s31, s31, 0
	s_lshr_b32 s9, s0, 8
	s_lshl_b32 s9, s9, 7
	s_and_b32 s1, s0, 127
	s_add_i32 s9, s9, s1
	s_lshl_b32 s9, s9, 2
	s_add_u32 s30, s30, s9
	s_addc_u32 s31, s31, 0
	s_add_u32 s34, s4, 0x3c90000
	s_addc_u32 s35, s5, 0
	s_add_u32 s34, s34, s8
	s_addc_u32 s35, s35, 0
	s_lshl_b32 s9, s0, 12
	s_add_u32 s34, s34, s9
	s_addc_u32 s35, s35, 0
	s_branch .Lpc_d158_done

.Lpc_d158_done:
.Lpc_a148_ok:
	s_waitcnt vmcnt(28)
	v_cvt_pk_bf16_f32 v140, v4, v8
	v_cvt_pk_bf16_f32 v141, v12, v16
	v_cvt_pk_bf16_f32 v142, v5, v9
	v_cvt_pk_bf16_f32 v143, v13, v17
	v_cvt_pk_bf16_f32 v144, v6, v10
	v_cvt_pk_bf16_f32 v145, v14, v18
	v_cvt_pk_bf16_f32 v146, v7, v11
	v_cvt_pk_bf16_f32 v147, v15, v19
	ds_write_b64 v137, v[140:141] offset:0
	ds_write_b64 v137, v[142:143] offset:264
	ds_write_b64 v137, v[144:145] offset:528
	ds_write_b64 v137, v[146:147] offset:792
	s_waitcnt lgkmcnt(0)
	s_barrier
	ds_read2_b64 v[148:151], v138 offset1:1
	ds_read2_b64 v[152:155], v138 offset0:2 offset1:3
	s_add_u32 s62, s32, 0x0
	s_addc_u32 s63, s33, 0
	s_waitcnt lgkmcnt(0)
	global_store_dwordx4 v136, v[148:151], s[62:63]
	global_store_dwordx4 v136, v[152:155], s[62:63] offset:16
	s_add_u32 s62, s30, 0x0
	s_addc_u32 s63, s31, 0
	global_load_dwordx4 v[4:7], v132, s[62:63] nt
	global_load_dwordx4 v[8:11], v133, s[62:63] nt
	global_load_dwordx4 v[12:15], v134, s[62:63] nt
	global_load_dwordx4 v[16:19], v135, s[62:63] nt
	s_waitcnt vmcnt(30)
	v_cvt_pk_bf16_f32 v140, v20, v24
	v_cvt_pk_bf16_f32 v141, v28, v32
	v_cvt_pk_bf16_f32 v142, v21, v25
	v_cvt_pk_bf16_f32 v143, v29, v33
	v_cvt_pk_bf16_f32 v144, v22, v26
	v_cvt_pk_bf16_f32 v145, v30, v34
	v_cvt_pk_bf16_f32 v146, v23, v27
	v_cvt_pk_bf16_f32 v147, v31, v35
	ds_write_b64 v137, v[140:141] offset:16896
	ds_write_b64 v137, v[142:143] offset:17160
	ds_write_b64 v137, v[144:145] offset:17424
	ds_write_b64 v137, v[146:147] offset:17688
	s_waitcnt lgkmcnt(0)
	s_barrier
	ds_read2_b64 v[148:151], v139 offset1:1
	ds_read2_b64 v[152:155], v139 offset0:2 offset1:3
	s_add_u32 s62, s32, 0x100
	s_addc_u32 s63, s33, 0
	s_waitcnt lgkmcnt(0)
	global_store_dwordx4 v136, v[148:151], s[62:63]
	global_store_dwordx4 v136, v[152:155], s[62:63] offset:16
	s_add_u32 s62, s30, 0x100000
	s_addc_u32 s63, s31, 0
	global_load_dwordx4 v[20:23], v132, s[62:63] nt
	global_load_dwordx4 v[24:27], v133, s[62:63] nt
	global_load_dwordx4 v[28:31], v134, s[62:63] nt
	global_load_dwordx4 v[32:35], v135, s[62:63] nt
	s_waitcnt vmcnt(32)
	v_cvt_pk_bf16_f32 v140, v36, v40
	v_cvt_pk_bf16_f32 v141, v44, v48
	v_cvt_pk_bf16_f32 v142, v37, v41
	v_cvt_pk_bf16_f32 v143, v45, v49
	v_cvt_pk_bf16_f32 v144, v38, v42
	v_cvt_pk_bf16_f32 v145, v46, v50
	v_cvt_pk_bf16_f32 v146, v39, v43
	v_cvt_pk_bf16_f32 v147, v47, v51
	ds_write_b64 v137, v[140:141] offset:0
	ds_write_b64 v137, v[142:143] offset:264
	ds_write_b64 v137, v[144:145] offset:528
	ds_write_b64 v137, v[146:147] offset:792
	s_waitcnt lgkmcnt(0)
	s_barrier
	ds_read2_b64 v[148:151], v138 offset1:1
	ds_read2_b64 v[152:155], v138 offset0:2 offset1:3
	s_add_u32 s62, s32, 0x200
	s_addc_u32 s63, s33, 0
	s_waitcnt lgkmcnt(0)
	global_store_dwordx4 v136, v[148:151], s[62:63]
	global_store_dwordx4 v136, v[152:155], s[62:63] offset:16
	s_add_u32 s62, s30, 0x200000
	s_addc_u32 s63, s31, 0
	global_load_dwordx4 v[36:39], v132, s[62:63] nt
	global_load_dwordx4 v[40:43], v133, s[62:63] nt
	global_load_dwordx4 v[44:47], v134, s[62:63] nt
	global_load_dwordx4 v[48:51], v135, s[62:63] nt
	s_waitcnt vmcnt(34)
	v_cvt_pk_bf16_f32 v140, v52, v56
	v_cvt_pk_bf16_f32 v141, v60, v64
	v_cvt_pk_bf16_f32 v142, v53, v57
	v_cvt_pk_bf16_f32 v143, v61, v65
	v_cvt_pk_bf16_f32 v144, v54, v58
	v_cvt_pk_bf16_f32 v145, v62, v66
	v_cvt_pk_bf16_f32 v146, v55, v59
	v_cvt_pk_bf16_f32 v147, v63, v67
	ds_write_b64 v137, v[140:141] offset:16896
	ds_write_b64 v137, v[142:143] offset:17160
	ds_write_b64 v137, v[144:145] offset:17424
	ds_write_b64 v137, v[146:147] offset:17688
	s_waitcnt lgkmcnt(0)
	s_barrier
	ds_read2_b64 v[148:151], v139 offset1:1
	ds_read2_b64 v[152:155], v139 offset0:2 offset1:3
	s_add_u32 s62, s32, 0x300
	s_addc_u32 s63, s33, 0
	s_waitcnt lgkmcnt(0)
	global_store_dwordx4 v136, v[148:151], s[62:63]
	global_store_dwordx4 v136, v[152:155], s[62:63] offset:16
	s_add_u32 s62, s30, 0x300000
	s_addc_u32 s63, s31, 0
	global_load_dwordx4 v[52:55], v132, s[62:63] nt
	global_load_dwordx4 v[56:59], v133, s[62:63] nt
	global_load_dwordx4 v[60:63], v134, s[62:63] nt
	global_load_dwordx4 v[64:67], v135, s[62:63] nt
	s_waitcnt vmcnt(36)
	v_cvt_pk_bf16_f32 v140, v68, v72
	v_cvt_pk_bf16_f32 v141, v76, v80
	v_cvt_pk_bf16_f32 v142, v69, v73
	v_cvt_pk_bf16_f32 v143, v77, v81
	v_cvt_pk_bf16_f32 v144, v70, v74
	v_cvt_pk_bf16_f32 v145, v78, v82
	v_cvt_pk_bf16_f32 v146, v71, v75
	v_cvt_pk_bf16_f32 v147, v79, v83
	ds_write_b64 v137, v[140:141] offset:0
	ds_write_b64 v137, v[142:143] offset:264
	ds_write_b64 v137, v[144:145] offset:528
	ds_write_b64 v137, v[146:147] offset:792
	s_waitcnt lgkmcnt(0)
	s_barrier
	ds_read2_b64 v[148:151], v138 offset1:1
	ds_read2_b64 v[152:155], v138 offset0:2 offset1:3
	s_add_u32 s62, s32, 0x400
	s_addc_u32 s63, s33, 0
	s_waitcnt lgkmcnt(0)
	global_store_dwordx4 v136, v[148:151], s[62:63]
	global_store_dwordx4 v136, v[152:155], s[62:63] offset:16
	s_add_u32 s62, s30, 0x400000
	s_addc_u32 s63, s31, 0
	global_load_dwordx4 v[68:71], v132, s[62:63] nt
	global_load_dwordx4 v[72:75], v133, s[62:63] nt
	global_load_dwordx4 v[76:79], v134, s[62:63] nt
	global_load_dwordx4 v[80:83], v135, s[62:63] nt
	s_waitcnt vmcnt(38)
	v_cvt_pk_bf16_f32 v140, v84, v88
	v_cvt_pk_bf16_f32 v141, v92, v96
	v_cvt_pk_bf16_f32 v142, v85, v89
	v_cvt_pk_bf16_f32 v143, v93, v97
	v_cvt_pk_bf16_f32 v144, v86, v90
	v_cvt_pk_bf16_f32 v145, v94, v98
	v_cvt_pk_bf16_f32 v146, v87, v91
	v_cvt_pk_bf16_f32 v147, v95, v99
	ds_write_b64 v137, v[140:141] offset:16896
	ds_write_b64 v137, v[142:143] offset:17160
	ds_write_b64 v137, v[144:145] offset:17424
	ds_write_b64 v137, v[146:147] offset:17688
	s_waitcnt lgkmcnt(0)
	s_barrier
	ds_read2_b64 v[148:151], v139 offset1:1
	ds_read2_b64 v[152:155], v139 offset0:2 offset1:3
	s_add_u32 s62, s32, 0x500
	s_addc_u32 s63, s33, 0
	s_waitcnt lgkmcnt(0)
	global_store_dwordx4 v136, v[148:151], s[62:63]
	global_store_dwordx4 v136, v[152:155], s[62:63] offset:16
	s_add_u32 s62, s30, 0x500000
	s_addc_u32 s63, s31, 0
	global_load_dwordx4 v[84:87], v132, s[62:63] nt
	global_load_dwordx4 v[88:91], v133, s[62:63] nt
	global_load_dwordx4 v[92:95], v134, s[62:63] nt
	global_load_dwordx4 v[96:99], v135, s[62:63] nt
	s_waitcnt vmcnt(40)
	v_cvt_pk_bf16_f32 v140, v100, v104
	v_cvt_pk_bf16_f32 v141, v108, v112
	v_cvt_pk_bf16_f32 v142, v101, v105
	v_cvt_pk_bf16_f32 v143, v109, v113
	v_cvt_pk_bf16_f32 v144, v102, v106
	v_cvt_pk_bf16_f32 v145, v110, v114
	v_cvt_pk_bf16_f32 v146, v103, v107
	v_cvt_pk_bf16_f32 v147, v111, v115
	ds_write_b64 v137, v[140:141] offset:0
	ds_write_b64 v137, v[142:143] offset:264
	ds_write_b64 v137, v[144:145] offset:528
	ds_write_b64 v137, v[146:147] offset:792
	s_waitcnt lgkmcnt(0)
	s_barrier
	ds_read2_b64 v[148:151], v138 offset1:1
	ds_read2_b64 v[152:155], v138 offset0:2 offset1:3
	s_add_u32 s62, s32, 0x600
	s_addc_u32 s63, s33, 0
	s_waitcnt lgkmcnt(0)
	global_store_dwordx4 v136, v[148:151], s[62:63]
	global_store_dwordx4 v136, v[152:155], s[62:63] offset:16
	s_add_u32 s62, s30, 0x600000
	s_addc_u32 s63, s31, 0
	global_load_dwordx4 v[100:103], v132, s[62:63] nt
	global_load_dwordx4 v[104:107], v133, s[62:63] nt
	global_load_dwordx4 v[108:111], v134, s[62:63] nt
	global_load_dwordx4 v[112:115], v135, s[62:63] nt
	s_waitcnt vmcnt(42)
	v_cvt_pk_bf16_f32 v140, v116, v120
	v_cvt_pk_bf16_f32 v141, v124, v128
	v_cvt_pk_bf16_f32 v142, v117, v121
	v_cvt_pk_bf16_f32 v143, v125, v129
	v_cvt_pk_bf16_f32 v144, v118, v122
	v_cvt_pk_bf16_f32 v145, v126, v130
	v_cvt_pk_bf16_f32 v146, v119, v123
	v_cvt_pk_bf16_f32 v147, v127, v131
	ds_write_b64 v137, v[140:141] offset:16896
	ds_write_b64 v137, v[142:143] offset:17160
	ds_write_b64 v137, v[144:145] offset:17424
	ds_write_b64 v137, v[146:147] offset:17688
	s_waitcnt lgkmcnt(0)
	s_barrier
	ds_read2_b64 v[148:151], v139 offset1:1
	ds_read2_b64 v[152:155], v139 offset0:2 offset1:3
	s_add_u32 s62, s32, 0x700
	s_addc_u32 s63, s33, 0
	s_waitcnt lgkmcnt(0)
	global_store_dwordx4 v136, v[148:151], s[62:63]
	global_store_dwordx4 v136, v[152:155], s[62:63] offset:16
	s_add_u32 s62, s30, 0x700000
	s_addc_u32 s63, s31, 0
	global_load_dwordx4 v[116:119], v132, s[62:63] nt
	global_load_dwordx4 v[120:123], v133, s[62:63] nt
	global_load_dwordx4 v[124:127], v134, s[62:63] nt
	global_load_dwordx4 v[128:131], v135, s[62:63] nt
	s_add_i32 s61, s61, -1
	s_cmp_eq_u32 s61, 0
	s_cbranch_scc1 .Lpc_end
.Lpc_loop:
	s_mov_b64 s[32:33], s[34:35]
	s_xor_b32 s58, s58, 1
	s_cmp_eq_u32 s58, 1
	s_cbranch_scc0 .Lpc_a448_new
	s_add_u32 s30, s30, 0x800000
	s_addc_u32 s31, s31, 0
	s_add_u32 s34, s34, 0x800
	s_addc_u32 s35, s35, 0
	s_branch .Lpc_a448_ok

.Lpc_d458_done:
.Lpc_a448_ok:
	s_waitcnt vmcnt(42)
	v_cvt_pk_bf16_f32 v140, v4, v8
	v_cvt_pk_bf16_f32 v141, v12, v16
	v_cvt_pk_bf16_f32 v142, v5, v9
	v_cvt_pk_bf16_f32 v143, v13, v17
	v_cvt_pk_bf16_f32 v144, v6, v10
	v_cvt_pk_bf16_f32 v145, v14, v18
	v_cvt_pk_bf16_f32 v146, v7, v11
	v_cvt_pk_bf16_f32 v147, v15, v19
	ds_write_b64 v137, v[140:141] offset:0
	ds_write_b64 v137, v[142:143] offset:264
	ds_write_b64 v137, v[144:145] offset:528
	ds_write_b64 v137, v[146:147] offset:792
	s_waitcnt lgkmcnt(0)
	s_barrier
	ds_read2_b64 v[148:151], v138 offset1:1
	ds_read2_b64 v[152:155], v138 offset0:2 offset1:3
	s_add_u32 s62, s32, 0x0
	s_addc_u32 s63, s33, 0
	s_waitcnt lgkmcnt(0)
	global_store_dwordx4 v136, v[148:151], s[62:63]
	global_store_dwordx4 v136, v[152:155], s[62:63] offset:16
	s_add_u32 s62, s30, 0x0
	s_addc_u32 s63, s31, 0
	global_load_dwordx4 v[4:7], v132, s[62:63] nt
	global_load_dwordx4 v[8:11], v133, s[62:63] nt
	global_load_dwordx4 v[12:15], v134, s[62:63] nt
	global_load_dwordx4 v[16:19], v135, s[62:63] nt
	s_waitcnt vmcnt(42)
	v_cvt_pk_bf16_f32 v140, v20, v24
	v_cvt_pk_bf16_f32 v141, v28, v32
	v_cvt_pk_bf16_f32 v142, v21, v25
	v_cvt_pk_bf16_f32 v143, v29, v33
	v_cvt_pk_bf16_f32 v144, v22, v26
	v_cvt_pk_bf16_f32 v145, v30, v34
	v_cvt_pk_bf16_f32 v146, v23, v27
	v_cvt_pk_bf16_f32 v147, v31, v35
	ds_write_b64 v137, v[140:141] offset:16896
	ds_write_b64 v137, v[142:143] offset:17160
	ds_write_b64 v137, v[144:145] offset:17424
	ds_write_b64 v137, v[146:147] offset:17688
	s_waitcnt lgkmcnt(0)
	s_barrier
	ds_read2_b64 v[148:151], v139 offset1:1
	ds_read2_b64 v[152:155], v139 offset0:2 offset1:3
	s_add_u32 s62, s32, 0x100
	s_addc_u32 s63, s33, 0
	s_waitcnt lgkmcnt(0)
	global_store_dwordx4 v136, v[148:151], s[62:63]
	global_store_dwordx4 v136, v[152:155], s[62:63] offset:16
	s_add_u32 s62, s30, 0x100000
	s_addc_u32 s63, s31, 0
	global_load_dwordx4 v[20:23], v132, s[62:63] nt
	global_load_dwordx4 v[24:27], v133, s[62:63] nt
	global_load_dwordx4 v[28:31], v134, s[62:63] nt
	global_load_dwordx4 v[32:35], v135, s[62:63] nt
	s_waitcnt vmcnt(42)
	v_cvt_pk_bf16_f32 v140, v36, v40
	v_cvt_pk_bf16_f32 v141, v44, v48
	v_cvt_pk_bf16_f32 v142, v37, v41
	v_cvt_pk_bf16_f32 v143, v45, v49
	v_cvt_pk_bf16_f32 v144, v38, v42
	v_cvt_pk_bf16_f32 v145, v46, v50
	v_cvt_pk_bf16_f32 v146, v39, v43
	v_cvt_pk_bf16_f32 v147, v47, v51
	ds_write_b64 v137, v[140:141] offset:0
	ds_write_b64 v137, v[142:143] offset:264
	ds_write_b64 v137, v[144:145] offset:528
	ds_write_b64 v137, v[146:147] offset:792
	s_waitcnt lgkmcnt(0)
	s_barrier
	ds_read2_b64 v[148:151], v138 offset1:1
	ds_read2_b64 v[152:155], v138 offset0:2 offset1:3
	s_add_u32 s62, s32, 0x200
	s_addc_u32 s63, s33, 0
	s_waitcnt lgkmcnt(0)
	global_store_dwordx4 v136, v[148:151], s[62:63]
	global_store_dwordx4 v136, v[152:155], s[62:63] offset:16
	s_add_u32 s62, s30, 0x200000
	s_addc_u32 s63, s31, 0
	global_load_dwordx4 v[36:39], v132, s[62:63] nt
	global_load_dwordx4 v[40:43], v133, s[62:63] nt
	global_load_dwordx4 v[44:47], v134, s[62:63] nt
	global_load_dwordx4 v[48:51], v135, s[62:63] nt
	s_waitcnt vmcnt(42)
	v_cvt_pk_bf16_f32 v140, v52, v56
	v_cvt_pk_bf16_f32 v141, v60, v64
	v_cvt_pk_bf16_f32 v142, v53, v57
	v_cvt_pk_bf16_f32 v143, v61, v65
	v_cvt_pk_bf16_f32 v144, v54, v58
	v_cvt_pk_bf16_f32 v145, v62, v66
	v_cvt_pk_bf16_f32 v146, v55, v59
	v_cvt_pk_bf16_f32 v147, v63, v67
	ds_write_b64 v137, v[140:141] offset:16896
	ds_write_b64 v137, v[142:143] offset:17160
	ds_write_b64 v137, v[144:145] offset:17424
	ds_write_b64 v137, v[146:147] offset:17688
	s_waitcnt lgkmcnt(0)
	s_barrier
	ds_read2_b64 v[148:151], v139 offset1:1
	ds_read2_b64 v[152:155], v139 offset0:2 offset1:3
	s_add_u32 s62, s32, 0x300
	s_addc_u32 s63, s33, 0
	s_waitcnt lgkmcnt(0)
	global_store_dwordx4 v136, v[148:151], s[62:63]
	global_store_dwordx4 v136, v[152:155], s[62:63] offset:16
	s_add_u32 s62, s30, 0x300000
	s_addc_u32 s63, s31, 0
	global_load_dwordx4 v[52:55], v132, s[62:63] nt
	global_load_dwordx4 v[56:59], v133, s[62:63] nt
	global_load_dwordx4 v[60:63], v134, s[62:63] nt
	global_load_dwordx4 v[64:67], v135, s[62:63] nt
	s_waitcnt vmcnt(42)
	v_cvt_pk_bf16_f32 v140, v68, v72
	v_cvt_pk_bf16_f32 v141, v76, v80
	v_cvt_pk_bf16_f32 v142, v69, v73
	v_cvt_pk_bf16_f32 v143, v77, v81
	v_cvt_pk_bf16_f32 v144, v70, v74
	v_cvt_pk_bf16_f32 v145, v78, v82
	v_cvt_pk_bf16_f32 v146, v71, v75
	v_cvt_pk_bf16_f32 v147, v79, v83
	ds_write_b64 v137, v[140:141] offset:0
	ds_write_b64 v137, v[142:143] offset:264
	ds_write_b64 v137, v[144:145] offset:528
	ds_write_b64 v137, v[146:147] offset:792
	s_waitcnt lgkmcnt(0)
	s_barrier
	ds_read2_b64 v[148:151], v138 offset1:1
	ds_read2_b64 v[152:155], v138 offset0:2 offset1:3
	s_add_u32 s62, s32, 0x400
	s_addc_u32 s63, s33, 0
	s_waitcnt lgkmcnt(0)
	global_store_dwordx4 v136, v[148:151], s[62:63]
	global_store_dwordx4 v136, v[152:155], s[62:63] offset:16
	s_add_u32 s62, s30, 0x400000
	s_addc_u32 s63, s31, 0
	global_load_dwordx4 v[68:71], v132, s[62:63] nt
	global_load_dwordx4 v[72:75], v133, s[62:63] nt
	global_load_dwordx4 v[76:79], v134, s[62:63] nt
	global_load_dwordx4 v[80:83], v135, s[62:63] nt
	s_waitcnt vmcnt(42)
	v_cvt_pk_bf16_f32 v140, v84, v88
	v_cvt_pk_bf16_f32 v141, v92, v96
	v_cvt_pk_bf16_f32 v142, v85, v89
	v_cvt_pk_bf16_f32 v143, v93, v97
	v_cvt_pk_bf16_f32 v144, v86, v90
	v_cvt_pk_bf16_f32 v145, v94, v98
	v_cvt_pk_bf16_f32 v146, v87, v91
	v_cvt_pk_bf16_f32 v147, v95, v99
	ds_write_b64 v137, v[140:141] offset:16896
	ds_write_b64 v137, v[142:143] offset:17160
	ds_write_b64 v137, v[144:145] offset:17424
	ds_write_b64 v137, v[146:147] offset:17688
	s_waitcnt lgkmcnt(0)
	s_barrier
	ds_read2_b64 v[148:151], v139 offset1:1
	ds_read2_b64 v[152:155], v139 offset0:2 offset1:3
	s_add_u32 s62, s32, 0x500
	s_addc_u32 s63, s33, 0
	s_waitcnt lgkmcnt(0)
	global_store_dwordx4 v136, v[148:151], s[62:63]
	global_store_dwordx4 v136, v[152:155], s[62:63] offset:16
	s_add_u32 s62, s30, 0x500000
	s_addc_u32 s63, s31, 0
	global_load_dwordx4 v[84:87], v132, s[62:63] nt
	global_load_dwordx4 v[88:91], v133, s[62:63] nt
	global_load_dwordx4 v[92:95], v134, s[62:63] nt
	global_load_dwordx4 v[96:99], v135, s[62:63] nt
	s_waitcnt vmcnt(42)
	v_cvt_pk_bf16_f32 v140, v100, v104
	v_cvt_pk_bf16_f32 v141, v108, v112
	v_cvt_pk_bf16_f32 v142, v101, v105
	v_cvt_pk_bf16_f32 v143, v109, v113
	v_cvt_pk_bf16_f32 v144, v102, v106
	v_cvt_pk_bf16_f32 v145, v110, v114
	v_cvt_pk_bf16_f32 v146, v103, v107
	v_cvt_pk_bf16_f32 v147, v111, v115
	ds_write_b64 v137, v[140:141] offset:0
	ds_write_b64 v137, v[142:143] offset:264
	ds_write_b64 v137, v[144:145] offset:528
	ds_write_b64 v137, v[146:147] offset:792
	s_waitcnt lgkmcnt(0)
	s_barrier
	ds_read2_b64 v[148:151], v138 offset1:1
	ds_read2_b64 v[152:155], v138 offset0:2 offset1:3
	s_add_u32 s62, s32, 0x600
	s_addc_u32 s63, s33, 0
	s_waitcnt lgkmcnt(0)
	global_store_dwordx4 v136, v[148:151], s[62:63]
	global_store_dwordx4 v136, v[152:155], s[62:63] offset:16
	s_add_u32 s62, s30, 0x600000
	s_addc_u32 s63, s31, 0
	global_load_dwordx4 v[100:103], v132, s[62:63] nt
	global_load_dwordx4 v[104:107], v133, s[62:63] nt
	global_load_dwordx4 v[108:111], v134, s[62:63] nt
	global_load_dwordx4 v[112:115], v135, s[62:63] nt
	s_waitcnt vmcnt(42)
	v_cvt_pk_bf16_f32 v140, v116, v120
	v_cvt_pk_bf16_f32 v141, v124, v128
	v_cvt_pk_bf16_f32 v142, v117, v121
	v_cvt_pk_bf16_f32 v143, v125, v129
	v_cvt_pk_bf16_f32 v144, v118, v122
	v_cvt_pk_bf16_f32 v145, v126, v130
	v_cvt_pk_bf16_f32 v146, v119, v123
	v_cvt_pk_bf16_f32 v147, v127, v131
	ds_write_b64 v137, v[140:141] offset:16896
	ds_write_b64 v137, v[142:143] offset:17160
	ds_write_b64 v137, v[144:145] offset:17424
	ds_write_b64 v137, v[146:147] offset:17688
	s_waitcnt lgkmcnt(0)
	s_barrier
	ds_read2_b64 v[148:151], v139 offset1:1
	ds_read2_b64 v[152:155], v139 offset0:2 offset1:3
	s_add_u32 s62, s32, 0x700
	s_addc_u32 s63, s33, 0
	s_waitcnt lgkmcnt(0)
	global_store_dwordx4 v136, v[148:151], s[62:63]
	global_store_dwordx4 v136, v[152:155], s[62:63] offset:16
	s_add_u32 s62, s30, 0x700000
	s_addc_u32 s63, s31, 0
	global_load_dwordx4 v[116:119], v132, s[62:63] nt
	global_load_dwordx4 v[120:123], v133, s[62:63] nt
	global_load_dwordx4 v[124:127], v134, s[62:63] nt
	global_load_dwordx4 v[128:131], v135, s[62:63] nt
	s_add_i32 s61, s61, -1
	s_cmp_lg_u32 s61, 0
	s_cbranch_scc1 .Lpc_loop
.Lpc_end:
	s_waitcnt vmcnt(0)
	s_barrier
	v_mov_b32_e32 v130, v0
.Lpc_skip:
	v_readlane_b32 s0, v251, 2
	s_cmpk_eq_i32 s0, 0x100
	s_cselect_b64 s[10:11], -1, 0
	s_and_b64 s[0:1], s[10:11], exec
	s_cselect_b32 s36, 15, 0
	s_movk_i32 s0, 0
	s_cselect_b32 s0, s0, 0x98c
	s_and_b32 s1, s36, 1
	s_bitcmp1_b32 s36, 0
	s_cselect_b64 s[4:5], -1, 0
	s_cmp_eq_u32 s1, 0
	s_movk_i32 s1, 0x1c9
	s_cselect_b32 s1, s1, 0x84
	s_not_b32 s6, s36
	s_lshl_b32 s6, s6, 7
	s_and_b32 s8, s6, 0x100
	s_and_b32 s9, s36, 4
	s_bitcmp1_b32 s36, 2
	s_cselect_b64 s[6:7], -1, 0
	s_cmp_eq_u32 s9, 0
	s_cselect_b32 s9, 0xb3, 0
	s_add_i32 s0, s8, s0
	s_add_i32 s29, s0, s1
	s_add_i32 s29, s29, s9
	v_readlane_b32 s0, v251, 3
	s_cmp_ge_i32 s0, s29
	s_barrier
	s_barrier
	s_cbranch_scc1 .LBB0_2768
	s_and_b64 s[0:1], s[10:11], exec
	v_readlane_b32 s1, v251, 3
	s_cselect_b32 s34, 0xd0, 0
	s_cmpk_lt_i32 s1, 0x84
	s_cbranch_scc1 .LBB0_73
	s_andn2_b64 vcc, exec, s[4:5]
	s_cbranch_vccnz .LBB0_54
	v_readlane_b32 s0, v251, 3
	s_add_i32 s13, s0, 0x145
	s_mov_b64 s[0:1], -1
	s_cbranch_execz .LBB0_55
	s_branch .LBB0_56
